# P2 stage B: KK^T/QK^T operand reads four rounds ahead through a 4-pair register ring with counted lgkmcnt; stacked
# baseline (speedup 1.0000x reference)
.LBB0_387:
	v_mov_b32_e32 v50, 0
	s_andn2_b64 vcc, exec, s[14:15]
	v_mov_b32_e32 v51, 0
	v_mov_b32_e32 v52, 0
	v_mov_b32_e32 v53, 0
	v_mov_b32_e32 v54, 0
	v_mov_b32_e32 v55, 0
	v_mov_b32_e32 v56, 0
	v_mov_b32_e32 v57, 0
	v_mov_b32_e32 v58, 0
	v_mov_b32_e32 v59, 0
	v_mov_b32_e32 v60, 0
	v_mov_b32_e32 v61, 0
	v_mov_b32_e32 v62, 0
	v_mov_b32_e32 v63, 0
	v_mov_b32_e32 v64, 0
	v_mov_b32_e32 v65, 0
	s_cbranch_vccnz .LBB0_389
	v_lshrrev_b32_e32 v1, 5, v2
	v_and_b32_e32 v2, 31, v186
	v_lshlrev_b32_e32 v5, 2, v186
	v_or_b32_e32 v4, s7, v2
	v_and_b32_e32 v12, 12, v5
	v_bfe_u32 v13, v186, 2, 2
	v_lshl_add_u32 v14, v4, 8, 0
	v_or_b32_e32 v2, s6, v2
	v_readlane_b32 s10, v254, 44
	s_waitcnt vmcnt(0)
	v_mov_b32_e32 v187, v68
	v_mov_b32_e32 v210, v69
	v_lshl_add_u32 v2, v2, 8, s10
	v_bitop3_b32 v252, v12, v1, v13 bitop3:0x36
	v_lshlrev_b32_e32 v252, 4, v252
	v_add_u32_e32 v253, v14, v252
	ds_read_b128 v[4:7], v253
	v_add_u32_e32 v252, v2, v252
	ds_read_b128 v[8:11], v252
	v_or_b32_e32 v252, 2, v1
	v_bitop3_b32 v252, v12, v252, v13 bitop3:0x36
	v_lshlrev_b32_e32 v252, 4, v252
	v_add_u32_e32 v253, v14, v252
	ds_read_b128 v[228:231], v253
	v_add_u32_e32 v252, v2, v252
	ds_read_b128 v[232:235], v252
	v_or_b32_e32 v252, 4, v1
	v_bitop3_b32 v252, v12, v252, v13 bitop3:0x36
	v_lshlrev_b32_e32 v252, 4, v252
	v_add_u32_e32 v253, v14, v252
	ds_read_b128 v[236:239], v253
	v_add_u32_e32 v252, v2, v252
	ds_read_b128 v[240:243], v252
	v_or_b32_e32 v252, 6, v1
	v_bitop3_b32 v252, v12, v252, v13 bitop3:0x36
	v_lshlrev_b32_e32 v252, 4, v252
	v_add_u32_e32 v253, v14, v252
	ds_read_b128 v[244:247], v253
	v_add_u32_e32 v252, v2, v252
	ds_read_b128 v[248:251], v252
	s_waitcnt lgkmcnt(6)
	v_mfma_f32_32x32x16_bf16 v[50:65], v[4:7], v[8:11], 0
	v_or_b32_e32 v252, 8, v1
	v_bitop3_b32 v252, v12, v252, v13 bitop3:0x36
	v_lshlrev_b32_e32 v252, 4, v252
	v_add_u32_e32 v253, v14, v252
	ds_read_b128 v[4:7], v253
	v_add_u32_e32 v252, v2, v252
	ds_read_b128 v[8:11], v252
	s_waitcnt lgkmcnt(6)
	v_mfma_f32_32x32x16_bf16 v[50:65], v[228:231], v[232:235], v[50:65]
	v_or_b32_e32 v252, 10, v1
	v_bitop3_b32 v252, v12, v252, v13 bitop3:0x36
	v_lshlrev_b32_e32 v252, 4, v252
	v_add_u32_e32 v253, v14, v252
	ds_read_b128 v[228:231], v253
	v_add_u32_e32 v252, v2, v252
	ds_read_b128 v[232:235], v252
	s_waitcnt lgkmcnt(6)
	v_mfma_f32_32x32x16_bf16 v[50:65], v[236:239], v[240:243], v[50:65]
	v_or_b32_e32 v252, 12, v1
	v_bitop3_b32 v252, v12, v252, v13 bitop3:0x36
	v_lshlrev_b32_e32 v252, 4, v252
	v_add_u32_e32 v253, v14, v252
	ds_read_b128 v[236:239], v253
	v_add_u32_e32 v252, v2, v252
	ds_read_b128 v[240:243], v252
	s_waitcnt lgkmcnt(6)
	v_mfma_f32_32x32x16_bf16 v[50:65], v[244:247], v[248:251], v[50:65]
	v_or_b32_e32 v252, 14, v1
	v_bitop3_b32 v252, v12, v252, v13 bitop3:0x36
	v_lshlrev_b32_e32 v252, 4, v252
	v_add_u32_e32 v253, v14, v252
	ds_read_b128 v[244:247], v253
	v_add_u32_e32 v252, v2, v252
	ds_read_b128 v[248:251], v252
	s_waitcnt lgkmcnt(6)
	v_mfma_f32_32x32x16_bf16 v[50:65], v[4:7], v[8:11], v[50:65]
	s_waitcnt lgkmcnt(4)
	v_mfma_f32_32x32x16_bf16 v[50:65], v[228:231], v[232:235], v[50:65]
	s_waitcnt lgkmcnt(2)
	v_mfma_f32_32x32x16_bf16 v[50:65], v[236:239], v[240:243], v[50:65]
	s_waitcnt lgkmcnt(0)
	v_mfma_f32_32x32x16_bf16 v[50:65], v[244:247], v[248:251], v[50:65]
